# sel tile: the first two exps sit between the rescale compare and its branch (recomputed on the rare rescale path), hiding the VALU-to-branch latency
# speedup vs baseline: 1.0117x; 1.0034x over previous
; __device__ __forceinline__ unsigned pk4_fp8(float a, float b, float c, float d) { unsigned w = 0u; w = __builtin_amdgcn_cvt_pk_fp8_f32(a, b, w, false); w = __builtin_amdgcn_cvt_pk_fp8_f32(c, d, w, true); return w; }
; __device__ __forceinline__ float xmax16(float v) { float a = v, b = v; PL_SWAP16(a, b); return fmaxf(a, b); }
; __device__ __forceinline__ float xmax32(float v) { float a = v, b = v; PL_SWAP32(a, b); return fmaxf(a, b); }
; #define LGKM_W(n) asm volatile("s_waitcnt lgkmcnt(" #n ")" ::: "memory"); SBAR()
; #define PV8_MM(dt) do { g.o[dt] = __builtin_amdgcn_mfma_f32_16x16x32_fp8_fp8(f.a[dt][0], b0, g.o[dt], 0, 0, 0); g.o[dt] = __builtin_amdgcn_mfma_f32_16x16x32_fp8_fp8(f.a[dt][1], b1, g.o[dt], 0, 0, 0); } while (0)
; template <class G> __device__ __forceinline__ void pv8_mm(G& g, const f32x4 (&s)[4], const VT8Frag& f) {
;     ...
;     unsigned pa[4];
; #pragma unroll
;     for (int T_ = 0; T_ < 4; ++T_) pa[T_] = pk4_fp8(s[T_][0], s[T_][1], s[T_][2], s[T_][3]);
;     const long b0 = (long)(((unsigned long long)pa[1] << 32) | pa[0]), b1 = (long)(((unsigned long long)pa[3] << 32) | pa[2]);
;     LGKM_W(14); PV8_MM(0); LGKM_W(12); PV8_MM(1); LGKM_W(10); PV8_MM(2); LGKM_W(8); PV8_MM(3);
;     LGKM_W(6); PV8_MM(4); LGKM_W(4); PV8_MM(5); LGKM_W(2); PV8_MM(6); LGKM_W(0); PV8_MM(7);
; template <class G> __device__ __forceinline__ void online_sm8(f32x4 (&s)[4], G& g, const float ref) {
;     float mx = s[0][0];
; #pragma unroll
;     for (int T_ = 0; T_ < 4; ++T_)
; #pragma unroll
;         for (int i = 0; i < 4; ++i) mx = fmaxf(mx, s[T_][i]);
;     const float t = mx + (ref - 5.f);
;     if (!__all(t <= g.m + SM_THR8)) {
;         const float mr = xmax32(xmax16(t));
;         const float mn = fmaxf(g.m, mr); const float al = __builtin_amdgcn_exp2f(g.m - mn); g.m = mn; g.l *= al;
; #pragma unroll
;         for (int dt = 0; dt < 8; ++dt) g.o[dt] = g.o[dt] * al;
;         const float d = ref - mn;
; #pragma unroll
;         for (int T_ = 0; T_ < 4; ++T_)
; #pragma unroll
;             for (int i = 0; i < 4; ++i) s[T_][i] += d;
;     }
;     float ps = 0.f;
; #pragma unroll
;     for (int T_ = 0; T_ < 4; ++T_)
; #pragma unroll
;         for (int i = 0; i < 4; ++i) { s[T_][i] = __builtin_amdgcn_exp2f(s[T_][i]); ps += s[T_][i]; }
;     g.l += ps;
.LBB0_1806:
	v_max_f32_e32 v18, v84, v85
	v_max3_f32 v18, v18, v86, v87
	v_max3_f32 v18, v18, v88, v89
	v_max3_f32 v18, v18, v90, v91
	v_max3_f32 v18, v18, v92, v93
	v_max3_f32 v18, v18, v94, v95
	v_max3_f32 v18, v18, v96, v97
	v_max3_f32 v114, v18, v98, v99
	v_cmp_nle_f32_e32 vcc, v114, v226
	v_exp_f32_e32 v240, v84
	v_exp_f32_e32 v241, v85
	s_cbranch_vccnz .Lsel_resc_g0
.Lsel_pa2_g0:
	v_exp_f32_e32 v242, v86
	v_exp_f32_e32 v243, v87
	v_exp_f32_e32 v244, v88
	v_exp_f32_e32 v245, v89
	v_exp_f32_e32 v246, v90
	v_exp_f32_e32 v247, v91
	s_waitcnt lgkmcnt(0)
	v_cvt_pk_fp8_f32 v84, v240, v241
	v_cvt_pk_fp8_f32 v85, v244, v245
	v_cvt_pk_fp8_f32 v84, v242, v243 op_sel:[0,0,1]
	v_cvt_pk_fp8_f32 v85, v246, v247 op_sel:[0,0,1]
	v_exp_f32_e32 v248, v92
	v_exp_f32_e32 v249, v93
	v_mfma_f32_16x16x32_fp8_fp8 v[80:83], v[134:135], v[84:85], v[80:83]
	v_exp_f32_e32 v250, v94
	v_mfma_f32_16x16x32_fp8_fp8 v[76:79], v[138:139], v[84:85], v[76:79]
	v_exp_f32_e32 v251, v95
	v_mfma_f32_16x16x32_fp8_fp8 v[72:75], v[142:143], v[84:85], v[72:75]
	v_exp_f32_e32 v252, v96
	v_mfma_f32_16x16x32_fp8_fp8 v[68:71], v[146:147], v[84:85], v[68:71]
	v_exp_f32_e32 v253, v97
	v_mfma_f32_16x16x32_fp8_fp8 v[64:67], v[118:119], v[84:85], v[64:67]
	v_exp_f32_e32 v254, v98
	v_mfma_f32_16x16x32_fp8_fp8 v[60:63], v[122:123], v[84:85], v[60:63]
	v_exp_f32_e32 v255, v99
	v_mfma_f32_16x16x32_fp8_fp8 v[56:59], v[126:127], v[84:85], v[56:59]
	v_mfma_f32_16x16x32_fp8_fp8 v[52:55], v[130:131], v[84:85], v[52:55]
	v_cvt_pk_fp8_f32 v86, v248, v249
	v_cvt_pk_fp8_f32 v87, v252, v253
	v_cvt_pk_fp8_f32 v86, v250, v251 op_sel:[0,0,1]
	v_cvt_pk_fp8_f32 v87, v254, v255 op_sel:[0,0,1]
	v_add_f32_e32 v240, v240, v241
	v_add_f32_e32 v242, v242, v243
	v_mfma_f32_16x16x32_fp8_fp8 v[80:83], v[136:137], v[86:87], v[80:83]
	v_add_f32_e32 v244, v244, v245
	v_add_f32_e32 v246, v246, v247
	v_mfma_f32_16x16x32_fp8_fp8 v[76:79], v[140:141], v[86:87], v[76:79]
	v_add_f32_e32 v248, v248, v249
	v_add_f32_e32 v250, v250, v251
	v_mfma_f32_16x16x32_fp8_fp8 v[72:75], v[144:145], v[86:87], v[72:75]
	v_add_f32_e32 v252, v252, v253
	v_add_f32_e32 v254, v254, v255
	v_mfma_f32_16x16x32_fp8_fp8 v[68:71], v[148:149], v[86:87], v[68:71]
	v_add_f32_e32 v240, v240, v242
	v_add_f32_e32 v244, v244, v246
	v_mfma_f32_16x16x32_fp8_fp8 v[64:67], v[120:121], v[86:87], v[64:67]
	v_add_f32_e32 v248, v248, v250
	v_add_f32_e32 v252, v252, v254
	v_mfma_f32_16x16x32_fp8_fp8 v[60:63], v[124:125], v[86:87], v[60:63]
	v_add_f32_e32 v240, v240, v244
	v_add_f32_e32 v248, v248, v252
	v_mfma_f32_16x16x32_fp8_fp8 v[56:59], v[128:129], v[86:87], v[56:59]
	v_add_f32_e32 v240, v240, v248
	v_add_f32_e32 v183, v183, v240
	v_mfma_f32_16x16x32_fp8_fp8 v[52:55], v[132:133], v[86:87], v[52:55]

; __device__ __forceinline__ unsigned pk4_fp8(float a, float b, float c, float d) { unsigned w = 0u; w = __builtin_amdgcn_cvt_pk_fp8_f32(a, b, w, false); w = __builtin_amdgcn_cvt_pk_fp8_f32(c, d, w, true); return w; }
; __device__ __forceinline__ float xmax16(float v) { float a = v, b = v; PL_SWAP16(a, b); return fmaxf(a, b); }
; __device__ __forceinline__ float xmax32(float v) { float a = v, b = v; PL_SWAP32(a, b); return fmaxf(a, b); }
; #define LGKM_W(n) asm volatile("s_waitcnt lgkmcnt(" #n ")" ::: "memory"); SBAR()
; #define PV8_MM(dt) do { g.o[dt] = __builtin_amdgcn_mfma_f32_16x16x32_fp8_fp8(f.a[dt][0], b0, g.o[dt], 0, 0, 0); g.o[dt] = __builtin_amdgcn_mfma_f32_16x16x32_fp8_fp8(f.a[dt][1], b1, g.o[dt], 0, 0, 0); } while (0)
; template <class G> __device__ __forceinline__ void pv8_mm(G& g, const f32x4 (&s)[4], const VT8Frag& f) {
;     ...
;     unsigned pa[4];
; #pragma unroll
;     for (int T_ = 0; T_ < 4; ++T_) pa[T_] = pk4_fp8(s[T_][0], s[T_][1], s[T_][2], s[T_][3]);
;     const long b0 = (long)(((unsigned long long)pa[1] << 32) | pa[0]), b1 = (long)(((unsigned long long)pa[3] << 32) | pa[2]);
;     LGKM_W(14); PV8_MM(0); LGKM_W(12); PV8_MM(1); LGKM_W(10); PV8_MM(2); LGKM_W(8); PV8_MM(3);
;     LGKM_W(6); PV8_MM(4); LGKM_W(4); PV8_MM(5); LGKM_W(2); PV8_MM(6); LGKM_W(0); PV8_MM(7);
; template <class G> __device__ __forceinline__ void online_sm8(f32x4 (&s)[4], G& g, const float ref) {
;     float mx = s[0][0];
; #pragma unroll
;     for (int T_ = 0; T_ < 4; ++T_)
; #pragma unroll
;         for (int i = 0; i < 4; ++i) mx = fmaxf(mx, s[T_][i]);
;     const float t = mx + (ref - 5.f);
;     if (!__all(t <= g.m + SM_THR8)) {
;         const float mr = xmax32(xmax16(t));
;         const float mn = fmaxf(g.m, mr); const float al = __builtin_amdgcn_exp2f(g.m - mn); g.m = mn; g.l *= al;
; #pragma unroll
;         for (int dt = 0; dt < 8; ++dt) g.o[dt] = g.o[dt] * al;
;         const float d = ref - mn;
; #pragma unroll
;         for (int T_ = 0; T_ < 4; ++T_)
; #pragma unroll
;             for (int i = 0; i < 4; ++i) s[T_][i] += d;
;     }
;     float ps = 0.f;
; #pragma unroll
;     for (int T_ = 0; T_ < 4; ++T_)
; #pragma unroll
;         for (int i = 0; i < 4; ++i) { s[T_][i] = __builtin_amdgcn_exp2f(s[T_][i]); ps += s[T_][i]; }
;     g.l += ps;
.LBB0_1812:
	v_max_f32_e32 v114, v84, v85
	v_max3_f32 v114, v114, v86, v87
	v_max3_f32 v114, v114, v88, v89
	v_max3_f32 v114, v114, v90, v91
	v_max3_f32 v114, v114, v92, v93
	v_max3_f32 v114, v114, v94, v95
	v_max3_f32 v114, v114, v96, v97
	v_max3_f32 v114, v114, v98, v99
	v_cmp_nle_f32_e32 vcc, v114, v227
	v_exp_f32_e32 v240, v84
	v_exp_f32_e32 v241, v85
	s_cbranch_vccnz .Lsel_resc_g1
.Lsel_pa2_g1:
	v_exp_f32_e32 v242, v86
	v_exp_f32_e32 v243, v87
	v_exp_f32_e32 v244, v88
	v_exp_f32_e32 v245, v89
	v_exp_f32_e32 v246, v90
	v_exp_f32_e32 v247, v91
	s_waitcnt lgkmcnt(0)
	v_cvt_pk_fp8_f32 v84, v240, v241
	v_cvt_pk_fp8_f32 v85, v244, v245
	v_cvt_pk_fp8_f32 v84, v242, v243 op_sel:[0,0,1]
	v_cvt_pk_fp8_f32 v85, v246, v247 op_sel:[0,0,1]
	v_exp_f32_e32 v248, v92
	v_exp_f32_e32 v249, v93
	v_mfma_f32_16x16x32_fp8_fp8 v[48:51], v[134:135], v[84:85], v[48:51]
	v_exp_f32_e32 v250, v94
	v_mfma_f32_16x16x32_fp8_fp8 v[44:47], v[138:139], v[84:85], v[44:47]
	v_exp_f32_e32 v251, v95
	v_mfma_f32_16x16x32_fp8_fp8 v[40:43], v[142:143], v[84:85], v[40:43]
	v_exp_f32_e32 v252, v96
	v_mfma_f32_16x16x32_fp8_fp8 v[36:39], v[146:147], v[84:85], v[36:39]
	v_exp_f32_e32 v253, v97
	v_mfma_f32_16x16x32_fp8_fp8 v[32:35], v[118:119], v[84:85], v[32:35]
	v_exp_f32_e32 v254, v98
	v_mfma_f32_16x16x32_fp8_fp8 v[28:31], v[122:123], v[84:85], v[28:31]
	v_exp_f32_e32 v255, v99
	v_mfma_f32_16x16x32_fp8_fp8 v[24:27], v[126:127], v[84:85], v[24:27]
	v_mfma_f32_16x16x32_fp8_fp8 v[20:23], v[130:131], v[84:85], v[20:23]
	v_cvt_pk_fp8_f32 v86, v248, v249
	v_cvt_pk_fp8_f32 v87, v252, v253
	v_cvt_pk_fp8_f32 v86, v250, v251 op_sel:[0,0,1]
	v_cvt_pk_fp8_f32 v87, v254, v255 op_sel:[0,0,1]
	v_add_f32_e32 v240, v240, v241
	v_add_f32_e32 v242, v242, v243
	v_mfma_f32_16x16x32_fp8_fp8 v[48:51], v[136:137], v[86:87], v[48:51]
	v_add_f32_e32 v244, v244, v245
	v_add_f32_e32 v246, v246, v247
	v_mfma_f32_16x16x32_fp8_fp8 v[44:47], v[140:141], v[86:87], v[44:47]
	v_add_f32_e32 v248, v248, v249
	v_add_f32_e32 v250, v250, v251
	v_mfma_f32_16x16x32_fp8_fp8 v[40:43], v[144:145], v[86:87], v[40:43]
	v_add_f32_e32 v252, v252, v253
	v_add_f32_e32 v254, v254, v255
	v_mfma_f32_16x16x32_fp8_fp8 v[36:39], v[148:149], v[86:87], v[36:39]
	v_add_f32_e32 v240, v240, v242
	v_add_f32_e32 v244, v244, v246
	v_mfma_f32_16x16x32_fp8_fp8 v[32:35], v[120:121], v[86:87], v[32:35]
	v_add_f32_e32 v248, v248, v250
	v_add_f32_e32 v252, v252, v254
	v_mfma_f32_16x16x32_fp8_fp8 v[28:31], v[124:125], v[86:87], v[28:31]
	v_add_f32_e32 v240, v240, v244
	v_add_f32_e32 v248, v248, v252
	v_mfma_f32_16x16x32_fp8_fp8 v[24:27], v[128:129], v[86:87], v[24:27]
	v_add_f32_e32 v240, v240, v248
	v_add_f32_e32 v182, v182, v240
	v_mfma_f32_16x16x32_fp8_fp8 v[20:23], v[132:133], v[86:87], v[20:23]
	s_branch .LBB0_1798
.LBB0_1808:
	v_exp_f32_e32 v240, v84
	v_exp_f32_e32 v241, v85
	s_branch .Lsel_pa2_g0
